# prep: block-id remap so the short weight-conversion blocks are dispatched first and the long x-streaming blocks last (clean tail)
# baseline (speedup 1.0000x reference)
_Z11prep_kernelPKfS0_S0_S0_S0_S0_S0_S0_S0_S0_S0_S0_S0_S0_S0_PDF16_S1_S1_Pf:
	s_add_i32 s3, s2, 0x800
	s_sub_i32 s4, s2, 0x960
	s_cmpk_lt_u32 s2, 0x960
	s_cselect_b32 s2, s3, s4
	s_cmpk_gt_u32 s2, 0x7ff
	s_mov_b64 s[4:5], -1
	s_cbranch_scc1 .LBB0_3
	s_andn2_b64 vcc, exec, s[4:5]
	s_cbranch_vccz .LBB0_6
